# mix1 light work lists: XCD-major workgroup index (guarded: applied only if every (XCD, role) counter equals G/16 after the first grid barrier)
# baseline (speedup 1.0000x reference)
; __device__ __forceinline__ unsigned xb_add(unsigned* p, unsigned v) { return __hip_atomic_fetch_add(p, v, __ATOMIC_RELAXED, __HIP_MEMORY_SCOPE_AGENT); }
; __device__ __forceinline__ unsigned xb_xcc_id() { return (unsigned)__builtin_amdgcn_s_getreg((3 << 11) | 20) & 0xFu; }
;     template <class T> __device__ __forceinline__ T* w(size_t off) const { return (T*)(p->ws + off); }
; __global__ void __launch_bounds__(NTHR, 2) mk_fwd(Params prm) {
;     ...
;     if (c.tid == 0) {
;         unsigned* ctl = c.w<unsigned>(WS_CTL);
;         const unsigned key = (xb_xcc_id() << 8) | ((unsigned)__builtin_amdgcn_s_getreg((7 << 11) | (8 << 6) | 4) & 0xFFu);
;         const unsigned prev = xb_add(&ctl[CW_CUKEY + key], 1u);
;         const unsigned role = prev & 1u;
;         const unsigned idx = xb_add(&ctl[CW_NROLE + 64 * role], 1u);
;         ((volatile unsigned*)smem)[100] = role; ((volatile unsigned*)smem)[101] = idx;
;     }
.LBB0_7:
	s_or_b64 exec, exec, s[12:13]
	s_mov_b64 s[10:11], src_shared_base
	s_waitcnt vmcnt(0)
	v_readfirstlane_b32 s10, v2
	v_mov_b32_e32 v2, 1
	s_nop 0
	v_add_u32_e32 v1, s10, v1
	v_and_b32_e32 v1, 1, v1
	v_lshlrev_b32_e32 v3, 8, v1
	global_atomic_add v4, v3, v2, s[4:5] offset:256 sc0
	s_getreg_b32 s96, hwreg(HW_REG_XCC_ID, 0, 4)
	s_and_b32 s96, s96, 15
	s_lshl_b32 s96, s96, 9
	v_lshl_add_u32 v5, v1, 8, s96
	v_add_u32_e32 v5, 0x80000, v5
	global_atomic_add v254, v5, v2, s[4:5] sc0
	v_mov_b32_e32 v2, 0x8d90
	v_mov_b32_e32 v3, s11
	flat_store_dword v[2:3], v1 sc0 sc1
	s_waitcnt vmcnt(0)
	v_mov_b32_e32 v2, 0x8d94
	flat_store_dword v[2:3], v4 sc0 sc1
	s_waitcnt vmcnt(0)

; __device__ __forceinline__ unsigned xb_ld(unsigned* p)              { return __hip_atomic_load(p, __ATOMIC_RELAXED, __HIP_MEMORY_SCOPE_AGENT); }
; __device__ __forceinline__ unsigned xb_add(unsigned* p, unsigned v) { return __hip_atomic_fetch_add(p, v, __ATOMIC_RELAXED, __HIP_MEMORY_SCOPE_AGENT); }
; __device__ __forceinline__ void xcd_barrier(const XcdBarrier& b) {
;     asm volatile("s_waitcnt vmcnt(0)" ::: "memory");
;     __syncthreads();
;     if (threadIdx.x == 0) {
;         unsigned* bar = b.bar;
;         __builtin_amdgcn_s_waitcnt(0);
;         unsigned nloc = b.st[0], nx = b.st[1];
;         if (nloc == 0u) { xcd_barrier_complete(bar, b.x, nloc, nx); b.st[0] = nloc; b.st[1] = nx; }
;         const unsigned old = xb_add(&bar[XB_XSUB(b.x)], 1u);
;         const unsigned gen = old / nloc;
;         if (old + 1u == (gen + 1u) * nloc) {
;             __builtin_amdgcn_fence(__ATOMIC_RELEASE, "agent");
;             asm volatile("s_waitcnt vmcnt(0)" ::: "memory");
;             const unsigned og = xb_add(&bar[XB_TOP], 1u);
;             const unsigned tg = og / nx;
;             if (og + 1u == (tg + 1u) * nx) xb_add(&bar[XB_TOPGEN], 1u);
;             else XB_SPIN(xb_ld(&bar[XB_TOPGEN]) == tg, bar);
;             __builtin_amdgcn_fence(__ATOMIC_ACQUIRE, "agent");
;             xb_add(&bar[XB_XGEN(b.x)], 1u);
;             asm volatile("s_waitcnt vmcnt(0)" ::: "memory");
;         } else {
;             XB_SPIN(xb_ld(&bar[XB_XGEN(b.x)]) == gen, bar);
;             __builtin_amdgcn_fence(__ATOMIC_ACQUIRE, "agent");
;             asm volatile("s_waitcnt vmcnt(0)" ::: "memory");
;         }
;     }
;     __syncthreads();
; }
; __device__ __forceinline__ void ph_mix1(Ctx& c, int layer, int bid, int G, unsigned char* lds, const volatile unsigned* rolew) {
;     const unsigned* ctl = c.w<unsigned>(WS_CTL);
;     int role = __builtin_amdgcn_readfirstlane((int)rolew[0]), idx = __builtin_amdgcn_readfirstlane((int)rolew[1]);
;     int nheavy = __builtin_amdgcn_readfirstlane((int)__hip_atomic_load(ctl + CW_NROLE, __ATOMIC_RELAXED, __HIP_MEMORY_SCOPE_AGENT)), nlight = __builtin_amdgcn_readfirstlane((int)__hip_atomic_load(ctl + CW_NROLE + 64, __ATOMIC_RELAXED, __HIP_MEMORY_SCOPE_AGENT));
;     if (nheavy < 1 || nlight < 1 || nheavy + nlight != G) {
;         nheavy = G / 2; nlight = G - nheavy; role = bid < nheavy ? 0 : 1; idx = role ? bid - nheavy : bid;
;     }
.Lxb_done:
	v_cmp_eq_u32_e32 vcc, 1, v255
	s_cbranch_vccz .Lxi_skipA
	ds_read_b32 v19, v146
	s_waitcnt lgkmcnt(0)
	v_cmp_eq_u32_e32 vcc, 1, v19
	s_cbranch_vccz .Lxi_skipA
	v_readlane_b32 s6, v252, 44
	v_readlane_b32 s7, v252, 45
	s_add_u32 s6, s6, 0x78c00
	s_addc_u32 s7, s7, 0
	s_lshr_b32 s15, s3, 4
	s_nop 2
	global_load_dword v2, v3, s[6:7] sc1
	global_load_dword v4, v3, s[6:7] offset:256 sc1
	global_load_dword v5, v3, s[6:7] offset:512 sc1
	global_load_dword v6, v3, s[6:7] offset:768 sc1
	global_load_dword v7, v3, s[6:7] offset:1024 sc1
	global_load_dword v8, v3, s[6:7] offset:1280 sc1
	global_load_dword v9, v3, s[6:7] offset:1536 sc1
	global_load_dword v10, v3, s[6:7] offset:1792 sc1
	global_load_dword v11, v3, s[6:7] offset:2048 sc1
	global_load_dword v12, v3, s[6:7] offset:2304 sc1
	global_load_dword v13, v3, s[6:7] offset:2560 sc1
	global_load_dword v14, v3, s[6:7] offset:2816 sc1
	global_load_dword v15, v3, s[6:7] offset:3072 sc1
	global_load_dword v16, v3, s[6:7] offset:3328 sc1
	global_load_dword v17, v3, s[6:7] offset:3584 sc1
	global_load_dword v18, v3, s[6:7] offset:3840 sc1
	s_waitcnt vmcnt(0)
	v_mov_b32_e32 v19, 0
	v_xor_b32_e32 v2, s15, v2
	v_or_b32_e32 v19, v19, v2
	v_xor_b32_e32 v4, s15, v4
	v_or_b32_e32 v19, v19, v4
	v_xor_b32_e32 v5, s15, v5
	v_or_b32_e32 v19, v19, v5
	v_xor_b32_e32 v6, s15, v6
	v_or_b32_e32 v19, v19, v6
	v_xor_b32_e32 v7, s15, v7
	v_or_b32_e32 v19, v19, v7
	v_xor_b32_e32 v8, s15, v8
	v_or_b32_e32 v19, v19, v8
	v_xor_b32_e32 v9, s15, v9
	v_or_b32_e32 v19, v19, v9
	v_xor_b32_e32 v10, s15, v10
	v_or_b32_e32 v19, v19, v10
	v_xor_b32_e32 v11, s15, v11
	v_or_b32_e32 v19, v19, v11
	v_xor_b32_e32 v12, s15, v12
	v_or_b32_e32 v19, v19, v12
	v_xor_b32_e32 v13, s15, v13
	v_or_b32_e32 v19, v19, v13
	v_xor_b32_e32 v14, s15, v14
	v_or_b32_e32 v19, v19, v14
	v_xor_b32_e32 v15, s15, v15
	v_or_b32_e32 v19, v19, v15
	v_xor_b32_e32 v16, s15, v16
	v_or_b32_e32 v19, v19, v16
	v_xor_b32_e32 v17, s15, v17
	v_or_b32_e32 v19, v19, v17
	v_xor_b32_e32 v18, s15, v18
	v_or_b32_e32 v19, v19, v18
	v_cmp_eq_u32_e32 vcc, 0, v19
	s_cbranch_vccz .Lxi_skipA
	s_getreg_b32 s16, hwreg(HW_REG_XCC_ID, 0, 4)
	s_and_b32 s16, s16, 15
	s_mul_i32 s16, s16, s15
	v_add_u32_e32 v19, s16, v254
	ds_write_b32 v148, v19
	s_waitcnt lgkmcnt(0)
